# speedup vs baseline: 1.0218x; 1.0218x over previous
.LBB0_3:
	s_load_dwordx8 s[8:15], s[0:1], 0x0
	v_and_b32_e32 v199, 15, v0
	v_lshrrev_b32_e32 v206, 4, v1
	s_cmpk_gt_u32 s38, 0x17f
	v_lshlrev_b32_e32 v205, 2, v206
	v_lshlrev_b32_e32 v194, 4, v206
	s_mul_i32 s37, s3, 0xc8
	v_lshl_or_b32 v204, s36, 4, v199
	s_cbranch_scc0 .LBB0_52
	s_add_i32 s39, s36, -6
	s_lshl_b32 s4, s33, 7
	s_waitcnt lgkmcnt(0)
	s_add_u32 s40, s20, s4
	s_addc_u32 s41, s21, 0
	s_add_u32 s6, s24, s4
	s_addc_u32 s7, s25, 0
	s_lshl_b32 s24, s39, 4
	v_or_b32_e32 v131, s24, v199
	v_min_u32_e32 v2, 0xc7, v131
	v_add_u32_e32 v2, s37, v2
	v_ashrrev_i32_e32 v3, 31, v2
	v_lshlrev_b64 v[2:3], 2, v[2:3]
	s_add_i32 s21, s36, -4
	v_lshl_add_u64 v[4:5], s[8:9], 0, v[2:3]
	v_lshl_add_u64 v[2:3], s[10:11], 0, v[2:3]
	v_lshl_or_b32 v201, s21, 4, v199
	global_load_dword v35, v[2:3], off
	v_min_u32_e32 v2, 0xc7, v201
	v_add_u32_e32 v2, s37, v2
	v_ashrrev_i32_e32 v3, 31, v2
	v_lshlrev_b64 v[2:3], 2, v[2:3]
	global_load_dword v34, v[4:5], off
	v_lshl_add_u64 v[4:5], s[8:9], 0, v[2:3]
	v_lshl_add_u64 v[2:3], s[10:11], 0, v[2:3]
	global_load_dword v36, v[4:5], off
	global_load_dword v37, v[2:3], off
	v_mov_b32_e32 v195, 0
	v_lshlrev_b32_e32 v42, 4, v0
	v_mov_b32_e32 v43, v195
	s_movk_i32 s20, 0x2000
	v_lshl_add_u64 v[10:11], s[34:35], 0, v[42:43]
	v_add_co_u32_e32 v20, vcc, s20, v10
	s_movk_i32 s42, 0x4000
	s_nop 0
	v_addc_co_u32_e32 v21, vcc, 0, v11, vcc
	v_lshlrev_b32_e32 v6, 6, v0
	v_add_co_u32_e32 v22, vcc, s42, v10
	s_movk_i32 s43, 0x6000
	v_and_b32_e32 v6, 0x7e00, v6
	v_mov_b32_e32 v7, v195
	v_addc_co_u32_e32 v23, vcc, 0, v11, vcc
	s_mov_b32 s5, 0
	global_load_dwordx4 v[2:5], v42, s[34:35]
	v_mov_b32_e32 v9, v195
	v_lshl_add_u64 v[12:13], s[18:19], 0, v[6:7]
	v_or_b32_e32 v8, 0x8000, v6
	v_lshl_add_u64 v[6:7], s[22:23], 0, v[6:7]
	v_add_co_u32_e32 v24, vcc, s43, v10
	global_load_dwordx4 v[118:121], v194, s[40:41]
	global_load_dwordx4 v[114:117], v194, s[40:41] offset:64
	v_addc_co_u32_e32 v25, vcc, 0, v11, vcc
	v_lshl_add_u64 v[26:27], v[12:13], 0, s[4:5]
	v_lshl_add_u64 v[28:29], s[18:19], 0, v[8:9]
	v_lshl_add_u64 v[30:31], v[6:7], 0, s[4:5]
	v_lshl_add_u64 v[32:33], s[22:23], 0, v[8:9]
	global_load_dwordx4 v[6:9], v[20:21], off
	global_load_dwordx4 v[10:13], v[22:23], off
	global_load_dwordx4 v[14:17], v[24:25], off
	v_and_b32_e32 v18, 0x70, v42
	v_mov_b32_e32 v19, v195
	v_lshl_add_u64 v[38:39], v[26:27], 0, v[18:19]
	v_lshl_add_u64 v[20:21], v[28:29], 0, s[4:5]
	v_lshl_add_u64 v[22:23], v[32:33], 0, s[4:5]
	v_lshl_add_u64 v[40:41], v[30:31], 0, v[18:19]
	global_load_dwordx4 v[126:129], v194, s[6:7]
	global_load_dwordx4 v[122:125], v194, s[6:7] offset:64
	v_lshl_add_u64 v[44:45], v[20:21], 0, v[18:19]
	v_lshl_add_u64 v[46:47], v[22:23], 0, v[18:19]
	global_load_dwordx4 v[18:21], v[38:39], off
	global_load_dwordx4 v[22:25], v[44:45], off
	global_load_dwordx4 v[26:29], v[40:41], off
	global_load_dwordx4 v[30:33], v[46:47], off
	s_movk_i32 s25, 0x2710
	s_add_i32 s20, s36, -2
	v_lshl_or_b32 v207, s20, 4, v199
	v_min_u32_e32 v43, 0xc7, v207
	v_and_b32_e32 v42, 48, v42
	v_lshlrev_b32_e32 v48, 2, v0
	s_waitcnt vmcnt(14)
	v_mad_u64_u32 v[34:35], s[4:5], v35, s25, v[34:35]
	v_ashrrev_i32_e32 v35, 31, v34
	v_lshlrev_b64 v[34:35], 9, v[34:35]
	s_waitcnt vmcnt(12)
	v_mad_u64_u32 v[36:37], s[4:5], v37, s25, v[36:37]
	v_ashrrev_i32_e32 v37, 31, v36
	v_lshlrev_b64 v[44:45], 9, v[36:37]
	v_lshl_add_u64 v[34:35], s[14:15], 0, v[34:35]
	v_lshl_add_u64 v[44:45], s[14:15], 0, v[44:45]
	v_lshl_add_u64 v[46:47], v[34:35], 0, v[194:195]
	v_lshl_add_u64 v[44:45], v[44:45], 0, v[194:195]
	global_load_dwordx4 v[34:37], v[46:47], off
	global_load_dwordx4 v[38:41], v[46:47], off offset:64
	global_load_dwordx4 v[54:57], v[46:47], off offset:128
	global_load_dwordx4 v[82:85], v[46:47], off offset:192
	global_load_dwordx4 v[86:89], v[46:47], off offset:256
	global_load_dwordx4 v[90:93], v[46:47], off offset:320
	global_load_dwordx4 v[94:97], v[46:47], off offset:384
	global_load_dwordx4 v[98:101], v[46:47], off offset:448
	global_load_dwordx4 v[158:161], v[44:45], off
	global_load_dwordx4 v[154:157], v[44:45], off offset:64
	global_load_dwordx4 v[150:153], v[44:45], off offset:128
	global_load_dwordx4 v[146:149], v[44:45], off offset:192
	global_load_dwordx4 v[66:69], v[44:45], off offset:256
	global_load_dwordx4 v[70:73], v[44:45], off offset:320
	global_load_dwordx4 v[74:77], v[44:45], off offset:384
	global_load_dwordx4 v[78:81], v[44:45], off offset:448
	v_add_u32_e32 v44, s37, v43
	v_ashrrev_i32_e32 v45, 31, v44
	v_lshlrev_b64 v[44:45], 2, v[44:45]
	v_lshl_add_u64 v[46:47], s[8:9], 0, v[44:45]
	v_lshl_add_u64 v[44:45], s[10:11], 0, v[44:45]
	global_load_dword v140, v[46:47], off
	global_load_dword v135, v[44:45], off
	v_min_u32_e32 v43, 0xc7, v204
	v_add_u32_e32 v44, s37, v43
	v_ashrrev_i32_e32 v45, 31, v44
	s_add_i32 s4, s24, 0x80
	v_lshlrev_b64 v[44:45], 2, v[44:45]
	v_or_b32_e32 v43, s4, v199
	v_lshl_add_u64 v[46:47], s[8:9], 0, v[44:45]
	v_lshl_add_u64 v[44:45], s[10:11], 0, v[44:45]
	v_min_u32_e32 v43, 0xc7, v43
	global_load_dword v133, v[44:45], off
	v_add_u32_e32 v44, s37, v43
	v_ashrrev_i32_e32 v45, 31, v44
	v_lshlrev_b64 v[44:45], 2, v[44:45]
	global_load_dword v130, v[46:47], off
	v_lshl_add_u64 v[46:47], s[8:9], 0, v[44:45]
	v_lshl_add_u64 v[44:45], s[10:11], 0, v[44:45]
	global_load_dword v134, v[44:45], off
	v_lshlrev_b32_e32 v45, 3, v0
	v_lshrrev_b32_e32 v43, 5, v0
	v_and_b32_e32 v44, 4, v0
	v_and_b32_e32 v45, 0xc0, v45
	v_or3_b32 v42, v42, v43, v45
	v_lshlrev_b32_e32 v43, 1, v44
	s_waitcnt vmcnt(32)
	v_cvt_pk_f16_f32 v2, v2, v3
	v_cvt_pk_f16_f32 v3, v4, v5
	v_lshl_or_b32 v42, v42, 4, v43
	s_waitcnt vmcnt(29)
	v_cvt_pk_f16_f32 v4, v6, v7
	v_cvt_pk_f16_f32 v5, v8, v9
	ds_write2st64_b64 v42, v[2:3], v[4:5] offset0:101 offset1:109
	s_waitcnt vmcnt(28)
	v_cvt_pk_f16_f32 v2, v10, v11
	v_cvt_pk_f16_f32 v3, v12, v13
	s_waitcnt vmcnt(27)
	v_cvt_pk_f16_f32 v4, v14, v15
	v_cvt_pk_f16_f32 v5, v16, v17
	ds_write2st64_b64 v42, v[2:3], v[4:5] offset0:117 offset1:125
	v_lshrrev_b32_e32 v4, 2, v0
	v_lshrrev_b32_e32 v2, 1, v0
	v_lshrrev_b32_e32 v3, 4, v0
	v_and_b32_e32 v4, 6, v4
	v_and_b32_e32 v2, 48, v2
	v_and_or_b32 v3, v3, 8, v4
	v_lshrrev_b32_e32 v4, 8, v0
	v_and_or_b32 v2, v0, 3, v2
	v_or_b32_e32 v4, v4, v44
	s_waitcnt vmcnt(24)
	v_cvt_f16_f32_e32 v5, v18
	v_lshlrev_b32_e32 v4, 10, v4
	v_lshlrev_b32_e32 v2, 4, v2
	v_or3_b32 v2, v2, v4, v3
	v_cvt_f16_f32_e32 v3, v19
	v_cvt_f16_f32_e32 v4, v20
	v_add_u32_e32 v2, 0x10a00, v2
	v_cvt_f16_f32_e32 v6, v21
	global_load_dword v132, v[46:47], off
	ds_write_b16 v2, v5
	ds_write_b16 v2, v3 offset:64
	ds_write_b16 v2, v4 offset:128
	ds_write_b16 v2, v6 offset:192
	s_waitcnt vmcnt(24)
	v_cvt_f16_f32_e32 v3, v22
	v_cvt_f16_f32_e32 v4, v23
	v_cvt_f16_f32_e32 v5, v24
	v_cvt_f16_f32_e32 v6, v25
	ds_write_b16 v2, v3 offset:2048
	ds_write_b16 v2, v4 offset:2112
	ds_write_b16 v2, v5 offset:2176
	ds_write_b16 v2, v6 offset:2240
	s_waitcnt vmcnt(23)
	v_cvt_f16_f32_e32 v3, v26
	v_cvt_f16_f32_e32 v4, v27
	v_cvt_f16_f32_e32 v5, v28
	v_cvt_f16_f32_e32 v6, v29
	ds_write_b16 v2, v3 offset:8192
	ds_write_b16 v2, v4 offset:8256
	ds_write_b16 v2, v5 offset:8320
	ds_write_b16 v2, v6 offset:8384
	s_waitcnt vmcnt(22)
	v_cvt_f16_f32_e32 v3, v30
	v_cvt_f16_f32_e32 v4, v31
	v_cvt_f16_f32_e32 v5, v32
	v_cvt_f16_f32_e32 v6, v33
	ds_write_b16 v2, v3 offset:10240
	ds_write_b16 v2, v4 offset:10304
	ds_write_b16 v2, v5 offset:10368
	ds_write_b16 v2, v6 offset:10432
	v_mov_b32_e32 v2, 0x10a00
	s_waitcnt lgkmcnt(0)
	s_barrier
	v_bfe_u32 v6, v1, 2, 2
	v_and_b32_e32 v7, 3, v1
	v_lshl_or_b32 v6, v7, 2, v6
	v_and_or_b32 v6, v1, 48, v6
	v_lshl_add_u32 v141, v6, 4, v2
	ds_read_b128 v[6:9], v141
	ds_read_b128 v[2:5], v141 offset:1024
	ds_read_b128 v[10:13], v141 offset:4096
	ds_read_b128 v[14:17], v141 offset:8192
	s_waitcnt vmcnt(21)
	v_cvt_pk_f16_f32 v102, v34, v35
	v_cvt_pk_f16_f32 v103, v36, v37
	s_waitcnt vmcnt(20)
	v_cvt_pk_f16_f32 v104, v38, v39
	v_cvt_pk_f16_f32 v105, v40, v41
	ds_read_b128 v[26:29], v141 offset:2048
	ds_read_b128 v[18:21], v141 offset:3072
	ds_read_b128 v[46:49], v141 offset:5120
	ds_read_b128 v[58:61], v141 offset:12288
	s_waitcnt lgkmcnt(7)
	v_mfma_f32_16x16x32_f16 v[38:41], v[6:9], v[102:105], 0
	s_waitcnt vmcnt(19)
	v_cvt_pk_f16_f32 v136, v54, v55
	v_cvt_pk_f16_f32 v137, v56, v57
	s_waitcnt vmcnt(18)
	v_cvt_pk_f16_f32 v138, v82, v83
	s_waitcnt lgkmcnt(5)
	v_mfma_f32_16x16x32_f16 v[106:109], v[10:13], v[102:105], 0
	v_cvt_pk_f16_f32 v139, v84, v85
	ds_read_b128 v[34:37], v141 offset:6144
	ds_read_b128 v[22:25], v141 offset:7168
	ds_read_b128 v[50:53], v141 offset:9216
	ds_read_b128 v[42:45], v141 offset:10240
	ds_read_b128 v[30:33], v141 offset:11264
	ds_read_b128 v[62:65], v141 offset:13312
	v_mfma_f32_16x16x32_f16 v[82:85], v[2:5], v[136:139], v[38:41]
	ds_read_b128 v[54:57], v141 offset:14336
	s_nop 1
	ds_read_b128 v[38:41], v141 offset:15360
	s_waitcnt vmcnt(4)
	v_mad_u64_u32 v[144:145], s[4:5], v135, s25, v[140:141]
	s_waitcnt lgkmcnt(12)
	v_mfma_f32_16x16x32_f16 v[110:113], v[14:17], v[102:105], 0
	v_cvt_pk_f16_f32 v140, v86, v87
	v_cvt_pk_f16_f32 v141, v88, v89
	v_cvt_pk_f16_f32 v142, v90, v91
	s_waitcnt lgkmcnt(8)
	v_mfma_f32_16x16x32_f16 v[102:105], v[58:61], v[102:105], 0
	v_cvt_pk_f16_f32 v143, v92, v93
	v_cvt_pk_f16_f32 v164, v98, v99
	v_cvt_pk_f16_f32 v165, v100, v101
	v_mfma_f32_16x16x32_f16 v[106:109], v[46:49], v[136:139], v[106:109]
	s_add_i32 s4, s24, 0xa0
	v_ashrrev_i32_e32 v145, 31, v144
	v_cvt_pk_f16_f32 v162, v94, v95
	v_mfma_f32_16x16x32_f16 v[98:101], v[26:29], v[140:143], v[82:85]
	v_cvt_pk_f16_f32 v163, v96, v97
	s_waitcnt lgkmcnt(5)
	v_mfma_f32_16x16x32_f16 v[86:89], v[50:53], v[136:139], v[110:113]
	v_lshlrev_b64 v[82:83], 9, v[144:145]
	v_lshl_add_u64 v[82:83], s[14:15], 0, v[82:83]
	v_lshl_add_u64 v[94:95], v[82:83], 0, v[194:195]
	s_waitcnt lgkmcnt(2)
	v_mfma_f32_16x16x32_f16 v[102:105], v[62:65], v[136:139], v[102:105]
	global_load_dwordx4 v[190:193], v[94:95], off
	global_load_dwordx4 v[186:189], v[94:95], off offset:64
	global_load_dwordx4 v[182:185], v[94:95], off offset:128
	global_load_dwordx4 v[178:181], v[94:95], off offset:192
	v_mfma_f32_16x16x32_f16 v[110:113], v[34:37], v[140:143], v[106:109]
	s_nop 2
	v_or_b32_e32 v106, s4, v199
	v_min_u32_e32 v135, 0xc7, v106
	v_mfma_f32_16x16x32_f16 v[106:109], v[18:21], v[162:165], v[98:101]
	s_movk_i32 s4, 0xc8
	v_cmp_gt_u32_e32 vcc, s4, v131
	s_nop 0
	v_add_u32_e32 v98, s37, v135
	v_ashrrev_i32_e32 v99, 31, v98
	v_mfma_f32_16x16x32_f16 v[136:139], v[42:45], v[140:143], v[86:89]
	global_load_dwordx4 v[82:85], v[94:95], off offset:256
	s_nop 1
	global_load_dwordx4 v[86:89], v[94:95], off offset:320
	global_load_dwordx4 v[90:93], v[94:95], off offset:384
	s_nop 0
	global_load_dwordx4 v[94:97], v[94:95], off offset:448
	s_waitcnt lgkmcnt(1)
	v_mfma_f32_16x16x32_f16 v[102:105], v[54:57], v[140:143], v[102:105]
	v_lshlrev_b64 v[140:141], 2, v[98:99]
	v_mfma_f32_16x16x32_f16 v[98:101], v[22:25], v[162:165], v[110:113]
	s_nop 2
	v_lshl_add_u64 v[110:111], s[8:9], 0, v[140:141]
	v_lshl_add_u64 v[140:141], s[10:11], 0, v[140:141]
	global_load_dword v200, v[110:111], off
	global_load_dword v208, v[140:141], off
	v_mfma_f32_16x16x32_f16 v[110:113], v[30:33], v[162:165], v[136:139]
	s_waitcnt lgkmcnt(0)
	v_mfma_f32_16x16x32_f16 v[102:105], v[38:41], v[162:165], v[102:105]
	s_and_saveexec_b64 s[4:5], vcc
	s_cbranch_execz .LBB0_6
	v_mul_f32_e32 v135, 0xbfb8aa3b, v118
	v_fmac_f32_e32 v135, 0xbfb8aa3b, v106
	v_exp_f32_e32 v106, v135
	v_mul_f32_e32 v135, 0x4038aa3b, v126
	v_fmac_f32_e32 v135, 0x4038aa3b, v110
	v_exp_f32_e32 v110, v135
	v_add_f32_e32 v106, 1.0, v106
	v_rcp_f32_e32 v135, v106
	s_movk_i32 s6, 0xca0
	v_add_f32_e32 v106, 1.0, v110
	v_mul_f32_e32 v110, 0xbfb8aa3b, v114
	v_fmac_f32_e32 v110, 0xbfb8aa3b, v98
	v_exp_f32_e32 v98, v110
	v_mul_f32_e32 v110, 0x4038aa3b, v122
	v_fmac_f32_e32 v110, 0x4038aa3b, v102
	v_exp_f32_e32 v102, v110
	v_add_f32_e32 v98, 1.0, v98
	v_rcp_f32_e32 v110, v98
	v_rcp_f32_e32 v106, v106
	v_add_f32_e32 v98, 1.0, v102
	v_mul_f32_e32 v102, 0xbfb8aa3b, v119
	v_fmac_f32_e32 v102, 0xbfb8aa3b, v107
	v_mul_f32_e32 v107, 0x4038aa3b, v127
	v_exp_f32_e32 v102, v102
	v_fmac_f32_e32 v107, 0x4038aa3b, v111
	v_exp_f32_e32 v107, v107
	v_rcp_f32_e32 v98, v98
	v_add_f32_e32 v102, 1.0, v102
	v_rcp_f32_e32 v111, v102
	v_add_f32_e32 v102, 1.0, v107
	v_rcp_f32_e32 v107, v102
	v_mul_f32_e32 v102, 0xbfb8aa3b, v115
	v_fmac_f32_e32 v102, 0xbfb8aa3b, v99
	v_exp_f32_e32 v99, v102
	v_mul_f32_e32 v102, 0x4038aa3b, v123
	v_fmac_f32_e32 v102, 0x4038aa3b, v103
	v_exp_f32_e32 v136, v102
	v_pk_fma_f32 v[102:103], v[106:107], -2.0, 1.0 op_sel_hi:[1,0,0]
	v_mul_f32_e32 v106, 0xbfb8aa3b, v120
	v_fmac_f32_e32 v106, 0xbfb8aa3b, v108
	v_mul_f32_e32 v107, 0x4038aa3b, v128
	v_exp_f32_e32 v106, v106
	v_fmac_f32_e32 v107, 0x4038aa3b, v112
	v_exp_f32_e32 v107, v107
	v_add_f32_e32 v99, 1.0, v99
	v_add_f32_e32 v106, 1.0, v106
	v_rcp_f32_e32 v108, v106
	v_add_f32_e32 v106, 1.0, v107
	v_mul_f32_e32 v107, 0xbfb8aa3b, v116
	v_fmac_f32_e32 v107, 0xbfb8aa3b, v100
	v_exp_f32_e32 v100, v107
	v_mul_f32_e32 v107, 0x4038aa3b, v124
	v_fmac_f32_e32 v107, 0x4038aa3b, v104
	v_exp_f32_e32 v104, v107
	v_add_f32_e32 v100, 1.0, v100
	v_rcp_f32_e32 v112, v100
	v_mul_f32_e32 v107, 0x4038aa3b, v129
	v_add_f32_e32 v100, 1.0, v104
	v_mul_f32_e32 v104, 0xbfb8aa3b, v121
	v_fmac_f32_e32 v104, 0xbfb8aa3b, v109
	v_exp_f32_e32 v104, v104
	v_fmac_f32_e32 v107, 0x4038aa3b, v113
	v_exp_f32_e32 v107, v107
	v_rcp_f32_e32 v106, v106
	v_add_f32_e32 v104, 1.0, v104
	v_rcp_f32_e32 v109, v104
	v_add_f32_e32 v104, 1.0, v107
	v_rcp_f32_e32 v107, v104
	v_mul_f32_e32 v104, 0x4038aa3b, v125
	v_fmac_f32_e32 v104, 0x4038aa3b, v105
	v_mul_f32_e32 v105, 0xbfb8aa3b, v117
	v_exp_f32_e32 v104, v104
	v_fmac_f32_e32 v105, 0xbfb8aa3b, v101
	v_exp_f32_e32 v113, v105
	v_rcp_f32_e32 v137, v99
	v_add_f32_e32 v99, 1.0, v136
	v_add_f32_e32 v101, 1.0, v104
	v_rcp_f32_e32 v99, v99
	v_rcp_f32_e32 v100, v100
	v_rcp_f32_e32 v101, v101
	v_pk_fma_f32 v[104:105], v[106:107], -2.0, 1.0 op_sel_hi:[1,0,0]
	v_add_f32_e32 v106, 1.0, v113
	v_rcp_f32_e32 v113, v106
	v_cvt_pk_f16_f32 v107, v102, v103
	v_lshlrev_b32_e32 v102, 3, v131
	v_cvt_pk_f16_f32 v106, v135, v111
	v_mad_u32_u24 v111, v206, s6, v102
	v_pk_fma_f32 v[98:99], v[98:99], -2.0, 1.0 op_sel_hi:[1,0,0]
	v_pk_fma_f32 v[100:101], v[100:101], -2.0, 1.0 op_sel_hi:[1,0,0]
	v_cvt_pk_f16_f32 v102, v108, v109
	v_cvt_pk_f16_f32 v103, v104, v105
	v_add_u32_e32 v104, 0x6400, v111
	ds_write2_b64 v104, v[106:107], v[102:103] offset0:32 offset1:234
	v_cvt_pk_f16_f32 v102, v110, v137
	v_cvt_pk_f16_f32 v103, v98, v99
	v_cvt_pk_f16_f32 v98, v112, v113
	v_cvt_pk_f16_f32 v99, v100, v101
	v_add_u32_e32 v100, 0x9600, v111
	ds_write2_b64 v100, v[102:103], v[98:99] offset0:48 offset1:250

.LBB0_52:
	s_and_b64 vcc, exec, s[4:5]
	s_cbranch_vccz .LBB0_77
	s_add_i32 s42, s36, -4
	s_waitcnt vmcnt(2)
	v_lshl_or_b32 v87, s42, 4, v199
	s_waitcnt lgkmcnt(0)
	s_add_i32 s24, s36, -2
	v_add_u32_e32 v2, s37, v87
	v_lshl_or_b32 v179, s24, 4, v199
	v_ashrrev_i32_e32 v3, 31, v2
	v_add_u32_e32 v6, s37, v179
	v_lshl_add_u64 v[4:5], v[2:3], 2, s[8:9]
	v_ashrrev_i32_e32 v7, 31, v6
	v_lshl_add_u64 v[6:7], v[6:7], 2, s[8:9]
	global_load_dword v36, v[4:5], off
	global_load_dword v38, v[6:7], off
	v_lshlrev_b32_e32 v40, 4, v0
	v_mov_b32_e32 v41, 0
	s_movk_i32 s4, 0x2000
	v_lshl_add_u64 v[16:17], s[34:35], 0, v[40:41]
	v_add_co_u32_e32 v18, vcc, s4, v16
	s_movk_i32 s5, 0x4000
	s_nop 0
	v_addc_co_u32_e32 v19, vcc, 0, v17, vcc
	v_add_u32_e32 v4, s37, v204
	v_add_co_u32_e32 v20, vcc, s5, v16
	s_movk_i32 s6, 0x6000
	v_ashrrev_i32_e32 v5, 31, v4
	v_addc_co_u32_e32 v21, vcc, 0, v17, vcc
	v_lshl_add_u64 v[8:9], v[4:5], 2, s[8:9]
	v_add_co_u32_e32 v16, vcc, s6, v16
	global_load_dword v42, v[8:9], off
	global_load_dwordx4 v[4:7], v40, s[34:35]
	v_addc_co_u32_e32 v17, vcc, 0, v17, vcc
	global_load_dwordx4 v[8:11], v[18:19], off
	global_load_dwordx4 v[12:15], v[20:21], off
	v_lshlrev_b32_e32 v3, 6, v0
	global_load_dwordx4 v[16:19], v[16:17], off
	v_and_b32_e32 v24, 0x7e00, v3
	v_mov_b32_e32 v25, v41
	s_mov_b32 s5, 0
	s_lshl_b32 s4, s33, 7
	v_lshl_add_u64 v[20:21], s[18:19], 0, v[24:25]
	v_and_b32_e32 v28, 0x70, v40
	v_mov_b32_e32 v29, v41
	v_lshl_add_u64 v[20:21], v[20:21], 0, s[4:5]
	v_lshl_add_u64 v[20:21], v[20:21], 0, v[28:29]
	global_load_dwordx4 v[20:23], v[20:21], off
	v_mov_b32_e32 v27, v41
	v_or_b32_e32 v26, 0x8000, v24
	v_lshl_add_u64 v[24:25], s[22:23], 0, v[24:25]
	v_lshl_add_u64 v[30:31], s[18:19], 0, v[26:27]
	v_lshl_add_u64 v[32:33], v[24:25], 0, s[4:5]
	v_lshl_add_u64 v[24:25], v[30:31], 0, s[4:5]
	v_lshl_add_u64 v[24:25], v[24:25], 0, v[28:29]
	v_lshl_add_u64 v[34:35], s[22:23], 0, v[26:27]
	global_load_dwordx4 v[24:27], v[24:25], off
	v_lshl_add_u64 v[44:45], v[32:33], 0, v[28:29]
	v_lshl_add_u64 v[30:31], v[34:35], 0, s[4:5]
	v_lshl_add_u64 v[46:47], v[30:31], 0, v[28:29]
	global_load_dwordx4 v[28:31], v[44:45], off
	global_load_dwordx4 v[32:35], v[46:47], off
	s_add_i32 s39, s36, 2
	s_waitcnt vmcnt(11)
	v_mov_b32_e32 v195, v41
	s_lshl_b32 s41, s39, 4
	s_add_i32 s4, s41, s37
	v_lshlrev_b32_e32 v3, 2, v0
	s_load_dwordx2 s[20:21], s[0:1], 0x70
	s_cmp_eq_u32 s33, 0
	s_waitcnt vmcnt(10)
	v_ashrrev_i32_e32 v37, 31, v36
	s_waitcnt vmcnt(9)
	v_ashrrev_i32_e32 v39, 31, v38
	v_lshlrev_b64 v[36:37], 9, v[36:37]
	v_lshlrev_b64 v[38:39], 9, v[38:39]
	v_lshl_add_u64 v[36:37], s[12:13], 0, v[36:37]
	v_lshl_add_u64 v[38:39], s[12:13], 0, v[38:39]
	v_lshl_add_u64 v[36:37], v[36:37], 0, v[194:195]
	v_lshl_add_u64 v[38:39], v[38:39], 0, v[194:195]
	global_load_dwordx4 v[66:69], v[36:37], off
	global_load_dwordx4 v[70:73], v[36:37], off offset:64
	global_load_dwordx4 v[74:77], v[36:37], off offset:128
	global_load_dwordx4 v[102:105], v[36:37], off offset:192
	global_load_dwordx4 v[110:113], v[36:37], off offset:256
	global_load_dwordx4 v[162:165], v[36:37], off offset:320
	global_load_dwordx4 v[166:169], v[36:37], off offset:384
	global_load_dwordx4 v[170:173], v[36:37], off offset:448
	global_load_dwordx4 v[142:145], v[38:39], off
	global_load_dwordx4 v[138:141], v[38:39], off offset:64
	global_load_dwordx4 v[134:137], v[38:39], off offset:128
	global_load_dwordx4 v[130:133], v[38:39], off offset:192
	global_load_dwordx4 v[122:125], v[38:39], off offset:256
	global_load_dwordx4 v[118:121], v[38:39], off offset:320
	global_load_dwordx4 v[90:93], v[38:39], off offset:384
	global_load_dwordx4 v[94:97], v[38:39], off offset:448
	v_add_u32_e32 v36, s4, v199
	v_add_u32_e32 v38, 0x80, v2
	v_ashrrev_i32_e32 v37, 31, v36
	v_ashrrev_i32_e32 v39, 31, v38
	v_lshl_add_u64 v[36:37], v[36:37], 2, s[8:9]
	v_lshl_add_u64 v[38:39], v[38:39], 2, s[8:9]
	global_load_dword v88, v[36:37], off
	global_load_dword v86, v[38:39], off
	v_lshlrev_b32_e32 v39, 3, v0
	v_lshrrev_b32_e32 v36, 5, v0
	v_and_b32_e32 v37, 4, v0
	v_and_b32_e32 v38, 48, v40
	v_and_b32_e32 v39, 0xc0, v39
	v_or3_b32 v36, v38, v36, v39
	v_lshlrev_b32_e32 v38, 1, v37
	s_waitcnt vmcnt(25)
	v_cvt_pk_f16_f32 v4, v4, v5
	v_cvt_pk_f16_f32 v5, v6, v7
	v_lshl_or_b32 v36, v36, 4, v38
	s_waitcnt vmcnt(24)
	v_cvt_pk_f16_f32 v6, v8, v9
	v_cvt_pk_f16_f32 v7, v10, v11
	ds_write2st64_b64 v36, v[4:5], v[6:7] offset0:101 offset1:109
	s_waitcnt vmcnt(23)
	v_cvt_pk_f16_f32 v4, v12, v13
	v_cvt_pk_f16_f32 v5, v14, v15
	s_waitcnt vmcnt(22)
	v_cvt_pk_f16_f32 v6, v16, v17
	v_cvt_pk_f16_f32 v7, v18, v19
	ds_write2st64_b64 v36, v[4:5], v[6:7] offset0:117 offset1:125
	v_lshrrev_b32_e32 v4, 1, v0
	v_and_b32_e32 v4, 48, v4
	v_lshrrev_b32_e32 v5, 2, v0
	v_and_or_b32 v3, v0, 3, v4
	v_lshrrev_b32_e32 v4, 4, v0
	v_and_b32_e32 v5, 6, v5
	v_and_or_b32 v4, v4, 8, v5
	v_lshrrev_b32_e32 v5, 8, v0
	v_or_b32_e32 v5, v5, v37
	s_waitcnt vmcnt(21)
	v_cvt_f16_f32_e32 v6, v20
	v_lshlrev_b32_e32 v5, 10, v5
	v_lshlrev_b32_e32 v3, 4, v3
	v_or3_b32 v3, v3, v5, v4
	v_cvt_f16_f32_e32 v4, v21
	v_cvt_f16_f32_e32 v5, v22
	v_add_u32_e32 v3, 0x10a00, v3
	v_cvt_f16_f32_e32 v7, v23
	ds_write_b16 v3, v6
	ds_write_b16 v3, v4 offset:64
	ds_write_b16 v3, v5 offset:128
	ds_write_b16 v3, v7 offset:192
	s_waitcnt vmcnt(20)
	v_cvt_f16_f32_e32 v4, v24
	v_cvt_f16_f32_e32 v5, v25
	v_cvt_f16_f32_e32 v6, v26
	v_cvt_f16_f32_e32 v7, v27
	ds_write_b16 v3, v4 offset:2048
	ds_write_b16 v3, v5 offset:2112
	ds_write_b16 v3, v6 offset:2176
	ds_write_b16 v3, v7 offset:2240
	s_waitcnt vmcnt(19)
	v_cvt_f16_f32_e32 v4, v28
	v_cvt_f16_f32_e32 v5, v29
	v_cvt_f16_f32_e32 v6, v30
	v_cvt_f16_f32_e32 v7, v31
	ds_write_b16 v3, v4 offset:8192
	ds_write_b16 v3, v5 offset:8256
	ds_write_b16 v3, v6 offset:8320
	ds_write_b16 v3, v7 offset:8384
	s_waitcnt vmcnt(18)
	v_cvt_f16_f32_e32 v4, v32
	v_cvt_f16_f32_e32 v5, v33
	v_cvt_f16_f32_e32 v6, v34
	v_ashrrev_i32_e32 v43, 31, v42
	v_cvt_f16_f32_e32 v7, v35
	ds_write_b16 v3, v4 offset:10240
	ds_write_b16 v3, v5 offset:10304
	ds_write_b16 v3, v6 offset:10368
	ds_write_b16 v3, v7 offset:10432
	v_lshlrev_b64 v[4:5], 9, v[42:43]
	v_lshl_add_u64 v[4:5], s[12:13], 0, v[4:5]
	s_waitcnt lgkmcnt(0)
	s_barrier
	v_lshl_add_u64 v[4:5], v[4:5], 0, v[194:195]
	global_load_dwordx4 v[158:161], v[4:5], off
	global_load_dwordx4 v[154:157], v[4:5], off offset:64
	global_load_dwordx4 v[150:153], v[4:5], off offset:128
	global_load_dwordx4 v[146:149], v[4:5], off offset:192
	global_load_dwordx4 v[126:129], v[4:5], off offset:256
	global_load_dwordx4 v[114:117], v[4:5], off offset:320
	global_load_dwordx4 v[106:109], v[4:5], off offset:384
	global_load_dwordx4 v[98:101], v[4:5], off offset:448
	v_add_u32_e32 v2, 0xa0, v2
	v_ashrrev_i32_e32 v3, 31, v2
	v_lshl_add_u64 v[2:3], v[2:3], 2, s[8:9]
	global_load_dword v178, v[2:3], off
	v_lshlrev_b32_e32 v10, 4, v1
	v_add_u32_e32 v11, 0xca00, v10
	ds_read_b128 v[30:33], v10 offset:51712
	ds_read_b128 v[22:25], v10 offset:52736
	ds_read_b128 v[18:21], v10 offset:53760
	ds_read_b128 v[14:17], v10 offset:54784
	ds_read_b128 v[46:49], v10 offset:55808
	ds_read_b128 v[34:37], v10 offset:56832
	ds_read_b128 v[26:29], v10 offset:57856
	ds_read_b128 v[2:5], v10 offset:58880
	ds_read_b128 v[54:57], v10 offset:59904
	ds_read_b128 v[50:53], v10 offset:60928
	ds_read_b128 v[38:41], v10 offset:61952
	ds_read_b128 v[6:9], v10 offset:62976
	ds_read_b128 v[62:65], v10 offset:64000
	ds_read_b128 v[58:61], v10 offset:65024
	ds_read_b128 v[42:45], v11 offset:14336
	ds_read_b128 v[10:13], v11 offset:15360
	s_waitcnt vmcnt(26)
	v_cvt_pk_f16_f32 v82, v66, v67
	v_cvt_pk_f16_f32 v83, v68, v69
	s_waitcnt vmcnt(25)
	v_cvt_pk_f16_f32 v84, v70, v71
	v_cvt_pk_f16_f32 v85, v72, v73
	s_cselect_b64 s[4:5], -1, 0
	s_cmp_lg_u32 s33, 0
	v_mov_b64_e32 v[66:67], v[82:83]
	s_waitcnt vmcnt(24)
	v_cvt_pk_f16_f32 v78, v74, v75
	v_cvt_pk_f16_f32 v79, v76, v77
	s_waitcnt vmcnt(23)
	v_cvt_pk_f16_f32 v80, v102, v103
	v_cvt_pk_f16_f32 v81, v104, v105
	s_waitcnt vmcnt(22)
	v_cvt_pk_f16_f32 v74, v110, v111
	v_cvt_pk_f16_f32 v75, v112, v113
	s_waitcnt vmcnt(21)
	v_cvt_pk_f16_f32 v76, v162, v163
	v_cvt_pk_f16_f32 v77, v164, v165
	s_waitcnt vmcnt(20)
	v_cvt_pk_f16_f32 v70, v166, v167
	v_cvt_pk_f16_f32 v71, v168, v169
	s_waitcnt vmcnt(19)
	v_cvt_pk_f16_f32 v72, v170, v171
	v_cvt_pk_f16_f32 v73, v172, v173
	s_cselect_b64 s[10:11], -1, 0
	s_and_b64 vcc, exec, s[4:5]
	v_mov_b64_e32 v[68:69], v[84:85]
	s_cbranch_vccnz .LBB0_55
	s_cmp_eq_u32 s33, 1
	s_cselect_b64 vcc, -1, 0
	s_cmp_eq_u32 s33, 2
	s_cselect_b64 s[6:7], -1, 0
	v_cndmask_b32_e64 v66, v70, v74, s[6:7]
	v_cndmask_b32_e64 v67, v71, v75, s[6:7]
	v_cndmask_b32_e64 v68, v72, v76, s[6:7]
	v_cndmask_b32_e64 v69, v73, v77, s[6:7]
	v_cndmask_b32_e32 v69, v69, v81, vcc
	v_cndmask_b32_e32 v68, v68, v80, vcc
	v_cndmask_b32_e32 v67, v67, v79, vcc
	v_cndmask_b32_e32 v66, v66, v78, vcc

.LBB0_82:
	s_and_b32 s0, s2, 3
	s_lshl_b32 s0, s0, s4
	v_or3_b32 v13, v14, s0, v13
	s_ashr_i32 s0, s2, 1
	s_and_b32 s0, s0, -16
	v_lshrrev_b32_e32 v11, 3, v0
	v_lshl_add_u32 v13, v13, 7, s0
	v_and_or_b32 v14, v11, 15, v13
	v_mov_b32_e32 v16, s16
	v_mov_b32_e32 v17, s17
	v_ashrrev_i32_e32 v15, 31, v14
	v_lshl_add_u64 v[14:15], v[14:15], 2, v[16:17]
	global_load_dword v13, v[14:15], off
	s_lshl_b32 s4, s33, 5
	v_cmp_gt_u32_e32 vcc, 32, v0
	s_and_saveexec_b64 s[0:1], vcc
	v_mov_b32_e32 v14, 0x14a00
	v_lshl_add_u32 v14, v0, 2, v14
	v_mov_b32_e32 v15, 0
	ds_write_b32 v14, v15
	s_or_b64 exec, exec, s[0:1]
	v_mov_b32_e32 v49, 0
	v_lshlrev_b32_e32 v48, 4, v0
	v_lshl_add_u64 v[14:15], s[34:35], 0, v[48:49]
	v_add_co_u32_e32 v28, vcc, 0x2000, v14
	global_load_dwordx4 v[16:19], v48, s[34:35]
	s_nop 0
	v_addc_co_u32_e32 v29, vcc, 0, v15, vcc
	v_add_co_u32_e32 v30, vcc, 0x4000, v14
	s_mov_b32 s1, 0
	s_nop 0
	v_addc_co_u32_e32 v31, vcc, 0, v15, vcc
	v_add_co_u32_e32 v14, vcc, 0x6000, v14
	global_load_dwordx4 v[20:23], v[28:29], off
	global_load_dwordx4 v[24:27], v[30:31], off
	v_addc_co_u32_e32 v15, vcc, 0, v15, vcc
	global_load_dwordx4 v[28:31], v[14:15], off
	v_lshlrev_b32_e32 v14, 6, v0
	v_and_b32_e32 v14, 0x7e00, v14
	v_mov_b32_e32 v15, v49
	v_lshl_add_u64 v[32:33], s[18:19], 0, v[14:15]
	s_lshl_b32 s0, s4, 2
	v_lshl_add_u64 v[32:33], v[32:33], 0, s[0:1]
	v_and_b32_e32 v44, 0x70, v48
	v_mov_b32_e32 v45, v49
	v_lshl_add_u64 v[32:33], v[32:33], 0, v[44:45]
	v_or_b32_e32 v46, 0x8000, v14
	v_mov_b32_e32 v47, v49
	global_load_dwordx4 v[32:35], v[32:33], off
	v_lshl_add_u64 v[36:37], s[18:19], 0, v[46:47]
	v_lshl_add_u64 v[14:15], s[22:23], 0, v[14:15]
	v_lshl_add_u64 v[36:37], v[36:37], 0, s[0:1]
	v_lshl_add_u64 v[14:15], v[14:15], 0, s[0:1]
	v_lshl_add_u64 v[36:37], v[36:37], 0, v[44:45]
	v_lshl_add_u64 v[14:15], v[14:15], 0, v[44:45]
	global_load_dwordx4 v[36:39], v[36:37], off
	v_lshlrev_b32_e32 v49, 3, v0
	global_load_dwordx4 v[40:43], v[14:15], off
	v_lshl_add_u64 v[14:15], s[22:23], 0, v[46:47]
	v_lshl_add_u64 v[14:15], v[14:15], 0, s[0:1]
	v_lshl_add_u64 v[14:15], v[14:15], 0, v[44:45]
	global_load_dwordx4 v[44:47], v[14:15], off
	v_lshrrev_b32_e32 v50, 1, v0
	v_lshrrev_b32_e32 v15, 5, v0
	v_and_b32_e32 v14, 4, v0
	v_lshrrev_b32_e32 v52, 2, v0
	v_lshrrev_b32_e32 v53, 8, v0
	v_and_b32_e32 v48, 48, v48
	v_and_b32_e32 v49, 0xc0, v49
	v_and_b32_e32 v50, 48, v50
	v_lshrrev_b32_e32 v51, 4, v0
	v_lshlrev_b32_e32 v54, 1, v14
	v_and_b32_e32 v52, 6, v52
	v_or_b32_e32 v53, v53, v14
	v_or3_b32 v15, v48, v15, v49
	v_and_or_b32 v48, v0, 3, v50
	v_and_or_b32 v49, v51, 8, v52
	v_lshlrev_b32_e32 v50, 10, v53
	v_lshl_or_b32 v15, v15, 4, v54
	v_lshlrev_b32_e32 v48, 4, v48
	v_or3_b32 v48, v50, v48, v49
	v_add_u32_e32 v48, 0x10a00, v48
	s_movk_i32 s0, 0x80
	v_cmp_gt_u32_e32 vcc, s0, v0
	s_waitcnt vmcnt(7)
	v_cvt_pk_f16_f32 v16, v16, v17
	v_cvt_pk_f16_f32 v17, v18, v19
	s_waitcnt vmcnt(6)
	v_cvt_pk_f16_f32 v18, v20, v21
	v_cvt_pk_f16_f32 v19, v22, v23
	ds_write2st64_b64 v15, v[16:17], v[18:19] offset0:101 offset1:109
	s_waitcnt vmcnt(5)
	v_cvt_pk_f16_f32 v16, v24, v25
	v_cvt_pk_f16_f32 v17, v26, v27
	s_waitcnt vmcnt(4)
	v_cvt_pk_f16_f32 v18, v28, v29
	v_cvt_pk_f16_f32 v19, v30, v31
	s_waitcnt vmcnt(3)
	v_cvt_f16_f32_e32 v20, v32
	v_cvt_f16_f32_e32 v21, v33
	v_cvt_f16_f32_e32 v22, v34
	v_cvt_f16_f32_e32 v23, v35
	s_waitcnt vmcnt(2)
	v_cvt_f16_f32_e32 v24, v36
	v_cvt_f16_f32_e32 v25, v37
	v_cvt_f16_f32_e32 v26, v38
	v_cvt_f16_f32_e32 v27, v39
	ds_write2st64_b64 v15, v[16:17], v[18:19] offset0:117 offset1:125
	ds_write_b16 v48, v20
	ds_write_b16 v48, v21 offset:64
	ds_write_b16 v48, v22 offset:128
	ds_write_b16 v48, v23 offset:192
	ds_write_b16 v48, v24 offset:2048
	ds_write_b16 v48, v25 offset:2112
	ds_write_b16 v48, v26 offset:2176
	ds_write_b16 v48, v27 offset:2240
	s_waitcnt vmcnt(1)
	v_cvt_f16_f32_e32 v15, v40
	v_cvt_f16_f32_e32 v16, v41
	v_cvt_f16_f32_e32 v17, v42
	v_cvt_f16_f32_e32 v18, v43
	ds_write_b16 v48, v15 offset:8192
	ds_write_b16 v48, v16 offset:8256
	ds_write_b16 v48, v17 offset:8320
	ds_write_b16 v48, v18 offset:8384
	s_waitcnt vmcnt(0)
	v_cvt_f16_f32_e32 v15, v44
	v_cvt_f16_f32_e32 v16, v45
	v_cvt_f16_f32_e32 v17, v46
	v_cvt_f16_f32_e32 v18, v47
	ds_write_b16 v48, v15 offset:10240
	ds_write_b16 v48, v16 offset:10304
	ds_write_b16 v48, v17 offset:10368
	ds_write_b16 v48, v18 offset:10432
	s_and_saveexec_b64 s[0:1], vcc
	s_cbranch_execz .LBB0_86
	v_cvt_f16_f32_e32 v13, v13
	v_lshl_or_b32 v18, s2, 7, v0
	v_mov_b32_e32 v16, s28
	v_mov_b32_e32 v17, s29
	v_ashrrev_i32_e32 v19, 31, v18
	v_lshl_add_u64 v[16:17], v[18:19], 1, v[16:17]
	global_store_short v[16:17], v13, off
